# RWKV scan wave: next-record ready-flag read hoisted ahead of the chain (both unrolled blocks); prep-wait removal and GEMM unit-boundary peel kept
# speedup vs baseline: 1.0066x; 1.0066x over previous
.LBB0_1016:
	s_or_b64 exec, exec, s[22:23]
	v_cvt_pk_bf16_f32 v64, v100, v101
	v_cvt_pk_bf16_f32 v65, v102, v103
	v_cvt_pk_bf16_f32 v66, v96, v97
	v_cvt_pk_bf16_f32 v67, v98, v99
	v_cvt_pk_bf16_f32 v68, v108, v109
	v_cvt_pk_bf16_f32 v69, v110, v111
	s_waitcnt lgkmcnt(14)
	v_mfma_f32_16x16x32_bf16 v[76:79], v[16:19], v[64:67], 0
	v_cvt_pk_bf16_f32 v70, v112, v113
	v_cvt_pk_bf16_f32 v71, v114, v115
	s_mul_i32 s1, s9, 0xcd
	v_mfma_f32_16x16x32_bf16 v[64:67], v[0:3], v[64:67], 0
	s_bfe_u32 s1, s1, 0x5000b
	s_mul_i32 s1, s1, 10
	s_sub_i32 s1, s9, s1
	v_mfma_f32_16x16x32_bf16 v[76:79], v[20:23], v[68:71], v[76:79]
	s_lshl_b32 s92, s8, 15
	s_and_b32 s21, s1, 0xff
	s_lshl_b32 s1, s21, 2
	v_mfma_f32_16x16x32_bf16 v[66:69], v[4:7], v[68:71], v[64:67]
	s_add_i32 s26, s1, 0
	s_nop 2
	v_cvt_pk_bf16_f32 v8, v76, v77
	v_cvt_pk_bf16_f32 v9, v78, v79
	v_lshl_add_u64 v[64:65], v[184:185], 0, s[92:93]
	s_add_i32 s26, s26, 0x1fa00
	v_mov_b32_e32 v226, s26
	ds_read_b32 v226, v226
	s_waitcnt lgkmcnt(14)
	v_mfma_f32_16x16x32_bf16 v[76:79], v[24:27], v[8:11], 0
	s_add_i32 s1, s8, 2
	s_mov_b32 s27, 0x400001
	s_nop 5
	v_cvt_pk_bf16_f32 v8, v76, v77
	v_cvt_pk_bf16_f32 v9, v78, v79
	s_waitcnt lgkmcnt(13)
	s_nop 0
	v_mfma_f32_16x16x32_bf16 v[66:69], v[28:31], v[8:11], v[66:69]
	s_waitcnt lgkmcnt(6)
	v_mfma_f32_16x16x32_bf16 v[154:157], v[44:47], v[8:11], v[100:103]
	s_waitcnt lgkmcnt(5)
	v_mfma_f32_16x16x32_bf16 v[150:153], v[48:51], v[8:11], v[96:99]
	s_nop 3
	v_cvt_pk_bf16_f32 v12, v66, v67
	global_store_short v[64:65], v12, off
	global_store_short_d16_hi v[64:65], v12, off offset:2048
	v_add_co_u32_e32 v12, vcc, s7, v64
	s_waitcnt lgkmcnt(4)
	v_mfma_f32_16x16x32_bf16 v[146:149], v[52:55], v[8:11], v[108:111]
	v_cvt_pk_bf16_f32 v66, v68, v69
	v_addc_co_u32_e32 v13, vcc, 0, v65, vcc
	s_waitcnt lgkmcnt(3)
	v_mfma_f32_16x16x32_bf16 v[142:145], v[60:63], v[8:11], v[112:115]
	global_store_short v[12:13], v66, off
	global_store_short_d16_hi v[12:13], v66, off offset:2048
	s_waitcnt lgkmcnt(0)
	v_cmp_eq_u32_e32 vcc, s1, v226
	s_cbranch_vccnz .LBB0_1024
	s_branch .LBB0_1018

.LBB0_1026:
	s_or_b64 exec, exec, s[22:23]
	s_mul_i32 s100, s1, 0xcd
	s_bfe_u32 s100, s100, 0x5000b
	s_mul_i32 s100, s100, 10
	s_sub_i32 s100, s1, s100
	s_and_b32 s100, s100, 0xff
	s_lshl_b32 s100, s100, 2
	s_add_i32 s100, s100, 0x1fa00
	v_mov_b32_e32 v227, s100
	ds_read_b32 v227, v227
	v_pk_mul_f32 v[156:157], v[58:59], v[156:157]
	v_pk_mul_f32 v[154:155], v[56:57], v[154:155]
	v_pk_mul_f32 v[152:153], v[42:43], v[152:153]
	v_pk_mul_f32 v[150:151], v[40:41], v[150:151]
	v_pk_mul_f32 v[168:169], v[34:35], v[144:145]
	v_pk_mul_f32 v[166:167], v[32:33], v[142:143]
	v_cvt_pk_bf16_f32 v142, v154, v155
	v_cvt_pk_bf16_f32 v143, v156, v157
	v_cvt_pk_bf16_f32 v144, v150, v151
	v_cvt_pk_bf16_f32 v145, v152, v153
	v_pk_mul_f32 v[164:165], v[38:39], v[148:149]
	v_pk_mul_f32 v[162:163], v[36:37], v[146:147]
	s_waitcnt lgkmcnt(15)
	v_mfma_f32_16x16x32_bf16 v[170:173], v[116:119], v[142:145], 0
	v_cvt_pk_bf16_f32 v146, v162, v163
	v_cvt_pk_bf16_f32 v147, v164, v165
	v_cvt_pk_bf16_f32 v148, v166, v167
	v_cvt_pk_bf16_f32 v149, v168, v169
	v_mfma_f32_16x16x32_bf16 v[142:145], v[100:103], v[142:145], 0
	s_lshl_b32 s92, s9, 15
	v_lshl_add_u64 v[8:9], v[184:185], 0, s[92:93]
	s_cmpk_gt_u32 s8, 0xfd
	v_mfma_f32_16x16x32_bf16 v[170:173], v[120:123], v[146:149], v[170:173]
	s_cselect_b64 s[22:23], -1, 0
	v_mfma_f32_16x16x32_bf16 v[222:225], v[96:99], v[146:149], v[142:145]
	s_nop 5
	v_cvt_pk_bf16_f32 v158, v170, v171
	v_cvt_pk_bf16_f32 v159, v172, v173
	v_mov_b64_e32 v[172:173], v[34:35]
	v_mov_b64_e32 v[170:171], v[32:33]
	s_waitcnt lgkmcnt(14)
	v_mfma_f32_16x16x32_bf16 v[142:145], v[112:115], v[158:161], 0
	s_nop 7
	v_cvt_pk_bf16_f32 v158, v142, v143
	v_cvt_pk_bf16_f32 v159, v144, v145
	s_waitcnt lgkmcnt(5)
	s_nop 0
	v_mfma_f32_16x16x32_bf16 v[142:145], v[104:107], v[158:161], v[150:153]
	v_mfma_f32_16x16x32_bf16 v[150:153], v[68:71], v[158:161], v[222:225]
	v_mfma_f32_16x16x32_bf16 v[146:149], v[108:111], v[158:161], v[154:157]
	s_waitcnt lgkmcnt(4)
	v_mfma_f32_16x16x32_bf16 v[154:157], v[92:95], v[158:161], v[162:165]
	s_nop 4
	v_cvt_pk_bf16_f32 v12, v150, v151
	v_cvt_pk_bf16_f32 v64, v152, v153
	global_store_short v[8:9], v12, off
	s_waitcnt lgkmcnt(3)
	v_mfma_f32_16x16x32_bf16 v[150:153], v[76:79], v[158:161], v[166:169]
	global_store_short_d16_hi v[8:9], v12, off offset:2048
	v_add_co_u32_e32 v12, vcc, 0x1000, v8
	s_nop 0
	v_mov_b64_e32 v[168:169], v[38:39]
	v_addc_co_u32_e32 v13, vcc, 0, v9, vcc
	v_mov_b64_e32 v[164:165], v[42:43]
	v_mov_b64_e32 v[160:161], v[58:59]
	s_and_b64 vcc, exec, s[22:23]
	v_mov_b64_e32 v[166:167], v[36:37]
	v_mov_b64_e32 v[162:163], v[40:41]
	v_mov_b64_e32 v[158:159], v[56:57]
	global_store_short v[12:13], v64, off
	global_store_short_d16_hi v[12:13], v64, off offset:2048
	s_cbranch_vccnz .LBB0_1013
	s_mul_i32 s9, s1, 0xcd
	s_bfe_u32 s9, s9, 0x5000b
	s_mul_i32 s9, s9, 10
	s_sub_i32 s9, s1, s9
	s_and_b32 s9, s9, 0xff
	s_lshl_b32 s21, s9, 2
	s_add_i32 s21, s21, 0
	s_add_i32 s21, s21, 0x1fa00
	s_add_i32 s8, s8, 3
	s_mov_b32 s30, 0x400001
	s_waitcnt lgkmcnt(0)
	v_cmp_eq_u32_e32 vcc, s8, v227
	s_cbranch_vccnz .LBB0_1012
	s_branch .LBB0_1029
